# speedup vs baseline: 1.0165x; 1.0039x over previous
_Z6k_gemmPKfS0_PK15HIP_vector_typeIjLj4EEPDF16_PKh:
	s_load_dwordx4 s[20:23], s[0:1], 0x0
	s_load_dwordx4 s[4:7], s[0:1], 0x10
	s_load_dwordx2 s[38:39], s[0:1], 0x20
	v_readfirstlane_b32 s8, v0
	v_and_b32_e32 v1, 63, v0
	s_nop 3
	s_lshr_b32 s8, s8, 6
	s_and_b32 s40, s2, 7
	s_lshr_b32 s41, s2, 3
	s_mul_i32 s18, s40, 0x187
	s_add_u32 s19, s18, 0x187
	s_min_u32 s19, s19, 0xc35
	s_sub_u32 s33, s19, s18
	s_sub_u32 s33, s33, 0x180
	s_lshl_b32 s33, s33, 2
	s_cmp_lt_u32 s41, s33
	s_cselect_b32 s44, 7, 6
	s_lshr_b32 s45, s41, 2
	s_add_u32 s45, s45, s18
	s_add_u32 s45, s45, 0x180
	s_lshl_b32 s45, s45, 4
	s_and_b32 s46, s41, 3
	s_lshl_b32 s46, s46, 2
	s_add_u32 s47, s45, s46
	s_mul_i32 s45, s47, 0x4b0
	s_lshl_b32 s46, s47, 8
	s_add_i32 s18, s18, s41
	s_cmp_eq_u32 s8, 0
	s_cselect_b32 s9, s44, 6
	s_add_i32 s11, s44, 4
	s_lshl_b32 s18, s18, 4
	s_lshl_b32 s19, s8, 2
	s_add_i32 s33, s18, s19
	s_mul_i32 s12, s33, 0x4b0
	s_lshl_b32 s32, s18, 8
	s_sub_u32 s32, s32, 0x100000
	s_mov_b32 s10, 0
	v_lshl_add_u32 v253, v1, 10, s33
	v_mov_b32_e32 v254, s47
	v_cmp_eq_u32_e32 vcc, 6, v1
	s_nop 1
	v_cndmask_b32_e32 v253, v253, v254, vcc
	v_mov_b32_e32 v247, 0
	v_cmp_gt_i32_e32 vcc, s9, v1
	s_mov_b32 s18, 0xc350
	v_cmp_gt_i32_e64 s[36:37], s18, v253
	s_and_b64 vcc, vcc, s[36:37]
	s_waitcnt lgkmcnt(0)
	s_and_saveexec_b64 s[36:37], vcc
	global_load_dword v247, v253, s[38:39]
	s_mov_b64 exec, s[36:37]
	s_mov_b32 s24, s22
	s_and_b32 s25, s23, 0xffff
	s_mov_b32 s26, 0x3938700
	s_mov_b32 s27, 0x20000
	s_and_b32 s21, s21, 0xffff
	s_mov_b32 s22, 0x3938700
	s_mov_b32 s23, 0x20000
	s_mov_b32 s28, s6
	s_and_b32 s29, s7, 0xffff
	s_mov_b32 s30, 0xc35000
	s_mov_b32 s31, 0x20000
	v_lshlrev_b32_e32 v238, 4, v1
	buffer_load_dwordx4 v[138:141], v238, s[20:23], s12 offen nt
	buffer_load_dwordx4 v[142:145], v238, s[24:27], s12 offen nt
	v_mul_u32_u24_e32 v253, 0x1746, v1
	v_lshrrev_b32_e32 v253, 16, v253
	v_min_u32_e32 v253, 3, v253
	v_mul_u32_u24_e32 v254, 11, v253
	v_sub_u32_e32 v254, v1, v254
	v_lshlrev_b32_e32 v240, 3, v253
	v_mul_u32_u24_e32 v249, 0x4b0, v253
	v_lshl_add_u32 v249, v254, 4, v249
	v_add_u32_e32 v249, 0x400, v249
	v_mov_b32_e32 v255, 0x80000000
	v_cmp_gt_u32_e64 s[34:35], 44, v1
	s_nop 1
	v_cndmask_b32_e64 v239, v255, v249, s[34:35]
	v_lshl_add_u32 v250, s8, 2, v253
	v_mul_u32_u24_e32 v250, 0x4e0, v250
	v_lshl_add_u32 v250, v254, 3, v250
	v_add_u32_e32 v242, 0x200, v250
	s_mul_i32 s18, s8, 0x1380
	v_lshl_add_u32 v241, v1, 3, s18
	v_and_b32_e32 v249, 15, v1
	v_lshrrev_b32_e32 v250, 4, v1
	v_mul_u32_u24_e32 v243, 0x4e0, v249
	v_lshl_add_u32 v243, v250, 4, v243
	v_mul_u32_u24_e32 v244, 0x440, v250
	v_lshl_add_u32 v244, v249, 1, v244
	s_lshl_b32 s18, s8, 6
	s_add_i32 s18, s18, 39936
	v_add_u32_e32 v244, s18, v244
	v_lshrrev_b32_e32 v249, 4, v0
	v_and_b32_e32 v250, 15, v0
	v_mul_u32_u24_e32 v245, 0x110, v249
	v_lshl_add_u32 v245, v250, 4, v245
	v_add_u32_e32 v245, 39936, v245
	v_lshlrev_b32_e32 v246, 8, v249
	v_lshl_add_u32 v246, v250, 4, v246
	s_lshl_b32 s18, s8, 12
	s_add_i32 s18, s18, 48640
	v_lshl_add_u32 v248, v1, 4, s18
	v_cmp_gt_u32_e32 vcc, 32, v0
	s_and_saveexec_b64 s[36:37], vcc
	v_mul_u32_u24_e32 v251, 0x4e00, v249
	v_mul_u32_u24_e32 v252, 0x4e0, v250
	v_add_u32_e32 v254, v251, v252
	v_mov_b32_e32 v250, 0
	v_mov_b32_e32 v251, 0
	v_mov_b32_e32 v252, 0
	v_mov_b32_e32 v253, 0
	ds_write_b128 v254, v[250:253] offset:1200
	s_mov_b64 exec, s[36:37]
	s_lshl_b32 s18, s8, 11
	v_lshl_add_u32 v253, v1, 4, s18
	v_add_u32_e32 v254, 0x22000, v253
	global_load_dwordx4 v[178:181], v254, s[4:5]
	global_load_dwordx4 v[182:185], v254, s[4:5] offset:1024
	v_add_u32_e32 v254, 0x2000, v254
	global_load_dwordx4 v[186:189], v254, s[4:5]
	global_load_dwordx4 v[190:193], v254, s[4:5] offset:1024
	v_mov_b32_e32 v236, v253
	s_waitcnt vmcnt(6)
	v_readlane_b32 s13, v247, s10
	s_add_u32 s14, s12, 0x4b0
	s_add_u32 s15, s12, 0x960
	s_add_u32 s16, s12, 0xe10
	s_nop 1
	s_and_b32 s18, s13, 0xff
	s_cmp_eq_u32 s18, 1
	s_cselect_b32 s42, s12, 0x80000000
	s_and_b32 s18, s13, 0xff00
	s_cmp_eq_u32 s18, 0x100
	s_cselect_b32 s14, s14, 0x80000000
	s_and_b32 s18, s13, 0xff0000
	s_cmp_eq_u32 s18, 0x10000
	s_cselect_b32 s15, s15, 0x80000000
	s_and_b32 s18, s13, 0xff000000
	s_cmp_eq_u32 s18, 0x1000000
	s_cselect_b32 s16, s16, 0x80000000
	v_lshrrev_b32_e64 v249, v240, s13
	v_and_b32_e32 v249, 0xff, v249
	v_cmp_eq_u32_e32 vcc, 1, v249
	s_nop 1
	v_cndmask_b32_e32 v254, v255, v239, vcc
	buffer_load_dwordx4 v[146:149], v238, s[20:23], s14 offen sc1 nt
	buffer_load_dwordx4 v[150:153], v238, s[24:27], s14 offen sc1 nt
	buffer_load_dwordx4 v[154:157], v238, s[20:23], s15 offen sc1 nt
	buffer_load_dwordx4 v[158:161], v238, s[24:27], s15 offen sc1 nt
	buffer_load_dwordx4 v[162:165], v238, s[20:23], s16 offen sc1 nt
	buffer_load_dwordx4 v[166:169], v238, s[24:27], s16 offen sc1 nt
	buffer_load_dwordx4 v[170:173], v254, s[20:23], s12 offen sc1 nt
	buffer_load_dwordx4 v[174:177], v254, s[24:27], s12 offen sc1 nt
	s_add_u32 s12, s12, 0x12c000
	s_add_u32 s32, s32, 0x40000
	s_mov_b32 s19, 0x80000000
	buffer_store_dwordx4 v[226:229], v246, s[28:31], s19 offen sc0 sc1
	s_mov_b32 s10, 1
	global_load_dwordx4 v[2:5], v236, s[4:5]
	global_load_dwordx4 v[6:9], v236, s[4:5] offset:1024
	v_add_u32_e32 v236, 0x2000, v236
	global_load_dwordx4 v[10:13], v236, s[4:5]
	global_load_dwordx4 v[14:17], v236, s[4:5] offset:1024
	v_add_u32_e32 v236, 0x2000, v236
	global_load_dwordx4 v[18:21], v236, s[4:5]
	global_load_dwordx4 v[22:25], v236, s[4:5] offset:1024
	v_add_u32_e32 v236, 0x2000, v236
	global_load_dwordx4 v[26:29], v236, s[4:5]
	global_load_dwordx4 v[30:33], v236, s[4:5] offset:1024
	v_add_u32_e32 v236, 0x2000, v236
	global_load_dwordx4 v[34:37], v236, s[4:5]
	global_load_dwordx4 v[38:41], v236, s[4:5] offset:1024
	v_add_u32_e32 v236, 0x2000, v236
	global_load_dwordx4 v[42:45], v236, s[4:5]
	global_load_dwordx4 v[46:49], v236, s[4:5] offset:1024
	v_add_u32_e32 v236, 0x2000, v236
	global_load_dwordx4 v[50:53], v236, s[4:5]
	global_load_dwordx4 v[54:57], v236, s[4:5] offset:1024
	v_add_u32_e32 v236, 0x2000, v236
	global_load_dwordx4 v[58:61], v236, s[4:5]
	global_load_dwordx4 v[62:65], v236, s[4:5] offset:1024
	v_add_u32_e32 v236, 0x2000, v236
	global_load_dwordx4 v[66:69], v236, s[4:5]
	global_load_dwordx4 v[70:73], v236, s[4:5] offset:1024
	v_add_u32_e32 v236, 0x2000, v236
	global_load_dwordx4 v[74:77], v236, s[4:5]
	global_load_dwordx4 v[78:81], v236, s[4:5] offset:1024
	v_add_u32_e32 v236, 0x2000, v236
	global_load_dwordx4 v[82:85], v236, s[4:5]
	global_load_dwordx4 v[86:89], v236, s[4:5] offset:1024
	v_add_u32_e32 v236, 0x2000, v236
	global_load_dwordx4 v[90:93], v236, s[4:5]
	global_load_dwordx4 v[94:97], v236, s[4:5] offset:1024
	v_add_u32_e32 v236, 0x2000, v236
	global_load_dwordx4 v[98:101], v236, s[4:5]
	global_load_dwordx4 v[102:105], v236, s[4:5] offset:1024
	v_add_u32_e32 v236, 0x2000, v236
	global_load_dwordx4 v[106:109], v236, s[4:5]
	global_load_dwordx4 v[110:113], v236, s[4:5] offset:1024
	v_add_u32_e32 v236, 0x2000, v236
	global_load_dwordx4 v[114:117], v236, s[4:5]
	global_load_dwordx4 v[118:121], v236, s[4:5] offset:1024
	v_add_u32_e32 v236, 0x2000, v236
	global_load_dwordx4 v[122:125], v236, s[4:5]
	global_load_dwordx4 v[126:129], v236, s[4:5] offset:1024
	v_add_u32_e32 v236, 0x2000, v236
	global_load_dwordx4 v[130:133], v236, s[4:5]
	global_load_dwordx4 v[134:137], v236, s[4:5] offset:1024
	s_waitcnt vmcnt(43)
	ds_write_b128 v248, v[178:181]
	ds_write_b128 v248, v[182:185] offset:1024
	ds_write_b128 v248, v[186:189] offset:2048
	ds_write_b128 v248, v[190:193] offset:3072
	s_waitcnt lgkmcnt(0)
	s_barrier
	s_branch .Lg_half1
